# speedup vs baseline: 1.0056x; 1.0056x over previous
.LBB0_16:
	s_cmp_gt_u32 s3, 4
	s_cselect_b64 vcc, -1, 0
	v_add_u32_e32 v180, 0xffff0000, v236
	s_and_b64 s[12:13], vcc, exec
	v_cndmask_b32_e32 v237, v180, v1, vcc
	s_cselect_b32 s13, s29, s37
	s_cselect_b32 s12, s28, s36
	s_cselect_b32 s15, 0x20000, 0x20000
	s_cselect_b32 s14, s16, 0x8000000
	s_waitcnt lgkmcnt(0)
	s_barrier
	s_cmp_lg_u32 s3, 2
	s_cbranch_scc1 .Lw03_ydone
	ds_read_b128 v[92:95], v248
	ds_read_b128 v[88:91], v248 offset:32
	ds_read_b128 v[84:87], v248 offset:64
	ds_read_b128 v[80:83], v248 offset:96
	ds_read_b128 v[76:79], v248 offset:128
	ds_read_b128 v[72:75], v248 offset:160
	ds_read_b128 v[68:71], v248 offset:192
	ds_read_b128 v[64:67], v248 offset:224
	ds_read2_b64 v[60:63], v249 offset1:2
	ds_read2_b64 v[56:59], v249 offset0:4 offset1:6
	ds_read2_b64 v[52:55], v249 offset0:8 offset1:10
	ds_read2_b64 v[48:51], v249 offset0:12 offset1:14
	s_waitcnt lgkmcnt(0)
.Lw03_ydone:
	s_cmp_eq_u32 s3, 6
	s_cbranch_scc1 .Lw03_mfma0

.Lw03_wdone:
	v_cvt_pk_f16_f32 v37, v140, v144
	v_cvt_pk_f16_f32 v36, v132, v136
	v_cvt_pk_f16_f32 v35, v124, v128
	v_cvt_pk_f16_f32 v34, v116, v120
	v_cvt_pk_f16_f32 v41, v141, v145
	v_cvt_pk_f16_f32 v40, v133, v137
	v_cvt_pk_f16_f32 v39, v125, v129
	v_cvt_pk_f16_f32 v38, v117, v121
	v_cvt_pk_f16_f32 v45, v142, v146
	v_cvt_pk_f16_f32 v44, v134, v138
	v_cvt_pk_f16_f32 v43, v126, v130
	v_cvt_pk_f16_f32 v42, v118, v122
	v_cvt_pk_f16_f32 v115, v143, v147
	v_cvt_pk_f16_f32 v114, v135, v139
	v_cvt_pk_f16_f32 v113, v127, v131
	v_cvt_pk_f16_f32 v112, v119, v123
	buffer_load_dwordx4 v[116:119], v237, s[12:15], 0 offen nt
	buffer_load_dwordx4 v[120:123], v237, s[12:15], 0 offen offset:512 nt
	buffer_load_dwordx4 v[124:127], v237, s[12:15], 0 offen offset:1024 nt
	buffer_load_dwordx4 v[128:131], v237, s[12:15], 0 offen offset:1536 nt
	buffer_load_dwordx4 v[132:135], v237, s[12:15], 0 offen offset:2048 nt
	buffer_load_dwordx4 v[136:139], v237, s[12:15], 0 offen offset:2560 nt
	buffer_load_dwordx4 v[140:143], v237, s[12:15], 0 offen offset:3072 nt
	buffer_load_dwordx4 v[144:147], v237, s[12:15], 0 offen offset:3584 nt
	ds_write_b128 v234, v[34:37] offset:32768
	ds_write_b128 v234, v[38:41] offset:33792
	ds_write_b128 v234, v[42:45] offset:34816
	ds_write_b128 v234, v[112:115] offset:35840
	s_cmp_eq_u32 s3, 6
	s_cbranch_scc1 .Lw03_both
.Lw03_mfma0:
	ds_read_b128 v[180:183], v235
	ds_read_b128 v[188:191], v233
	ds_read_b128 v[192:195], v233 offset:1024
	ds_read_b128 v[184:187], v235 offset:4096
	s_waitcnt lgkmcnt(2)
	v_mfma_f32_32x32x16_f16 v[18:33], v[180:183], v[188:191], v[18:33]
	s_waitcnt lgkmcnt(1)
	v_mfma_f32_32x32x16_f16 v[2:17], v[180:183], v[192:195], v[2:17]
	ds_read_b128 v[188:191], v233 offset:4096
	ds_read_b128 v[192:195], v233 offset:5120
	s_waitcnt lgkmcnt(1)
	v_mfma_f32_32x32x16_f16 v[18:33], v[184:187], v[188:191], v[18:33]
	s_waitcnt lgkmcnt(0)
	v_mfma_f32_32x32x16_f16 v[2:17], v[184:187], v[192:195], v[2:17]
	ds_read_b128 v[188:191], v235 offset:8192
	ds_read_b128 v[196:199], v233 offset:8192
	ds_read_b128 v[200:203], v233 offset:9216
	ds_read_b128 v[192:195], v235 offset:12288
	s_waitcnt lgkmcnt(2)
	v_mfma_f32_32x32x16_f16 v[18:33], v[188:191], v[196:199], v[18:33]
	s_waitcnt lgkmcnt(1)
	v_mfma_f32_32x32x16_f16 v[2:17], v[188:191], v[200:203], v[2:17]
	ds_read_b128 v[196:199], v233 offset:12288
	ds_read_b128 v[200:203], v233 offset:13312
	s_waitcnt lgkmcnt(1)
	v_mfma_f32_32x32x16_f16 v[18:33], v[192:195], v[196:199], v[18:33]
	s_waitcnt lgkmcnt(0)
	v_mfma_f32_32x32x16_f16 v[2:17], v[192:195], v[200:203], v[2:17]
	ds_read_b128 v[196:199], v235 offset:16384
	ds_read_b128 v[204:207], v233 offset:16384
	ds_read_b128 v[208:211], v233 offset:17408
	ds_read_b128 v[200:203], v235 offset:20480
	s_waitcnt lgkmcnt(2)
	v_mfma_f32_32x32x16_f16 v[18:33], v[196:199], v[204:207], v[18:33]
	s_waitcnt lgkmcnt(1)
	v_mfma_f32_32x32x16_f16 v[2:17], v[196:199], v[208:211], v[2:17]
	ds_read_b128 v[204:207], v233 offset:20480
	ds_read_b128 v[208:211], v233 offset:21504
	s_waitcnt lgkmcnt(1)
	v_mfma_f32_32x32x16_f16 v[18:33], v[200:203], v[204:207], v[18:33]
	s_waitcnt lgkmcnt(0)
	v_mfma_f32_32x32x16_f16 v[2:17], v[200:203], v[208:211], v[2:17]
	ds_read_b128 v[204:207], v235 offset:24576
	ds_read_b128 v[238:241], v233 offset:24576
	ds_read_b128 v[242:245], v233 offset:25600
	ds_read_b128 v[208:211], v235 offset:28672
	s_waitcnt lgkmcnt(2)
	v_mfma_f32_32x32x16_f16 v[18:33], v[204:207], v[238:241], v[18:33]
	s_waitcnt lgkmcnt(1)
	v_mfma_f32_32x32x16_f16 v[2:17], v[204:207], v[242:245], v[2:17]
	ds_read_b128 v[238:241], v233 offset:28672
	ds_read_b128 v[242:245], v233 offset:29696
	s_waitcnt lgkmcnt(1)
	v_mfma_f32_32x32x16_f16 v[18:33], v[208:211], v[238:241], v[18:33]
	s_waitcnt lgkmcnt(0)
	v_mfma_f32_32x32x16_f16 v[2:17], v[208:211], v[242:245], v[2:17]
	s_cmp_eq_u32 s3, 6
	s_cbranch_scc1 .Lw03_stage
.Lw03_both:
	s_waitcnt lgkmcnt(0)
	s_cmp_gt_u32 s3, 5
	s_cselect_b64 s[12:13], -1, 0
	s_and_b64 vcc, exec, s[12:13]
	s_barrier
	s_cbranch_vccnz .LBB0_15
	s_waitcnt vmcnt(8)
	v_cvt_pk_f16_f32 v241, v172, v176
	v_cvt_pk_f16_f32 v240, v160, v168
	v_cvt_pk_f16_f32 v239, v164, v156
	v_cvt_pk_f16_f32 v238, v148, v152
	ds_write_b128 v234, v[238:241]
	v_cvt_pk_f16_f32 v241, v173, v177
	v_cvt_pk_f16_f32 v240, v161, v169
	v_cvt_pk_f16_f32 v239, v165, v157
	v_cvt_pk_f16_f32 v238, v149, v153
	ds_write_b128 v234, v[238:241] offset:1024
	v_cvt_pk_f16_f32 v241, v174, v178
	v_cvt_pk_f16_f32 v240, v162, v170
	v_cvt_pk_f16_f32 v239, v166, v158
	v_cvt_pk_f16_f32 v238, v150, v154
	v_cvt_pk_f16_f32 v161, v175, v179
	v_cvt_pk_f16_f32 v160, v163, v171
	v_cvt_pk_f16_f32 v159, v167, v159
	v_cvt_pk_f16_f32 v158, v151, v155
	ds_write_b128 v234, v[238:241] offset:2048
	ds_write_b128 v234, v[158:161] offset:3072
	s_cmp_lg_u32 s3, 0
	s_cbranch_scc1 .LBB0_15
	v_cvt_pk_f16_f32 v48, v48, v49
	v_cvt_pk_f16_f32 v49, v50, v51
	ds_write_b64 v246, v[48:49]
	v_cvt_pk_f16_f32 v80, v80, v81
	v_cvt_pk_f16_f32 v81, v82, v83
	ds_write_b64 v246, v[80:81] offset:34816
	v_cvt_pk_f16_f32 v52, v52, v53
	v_cvt_pk_f16_f32 v53, v54, v55
	ds_write_b64 v246, v[52:53] offset:4352
	v_cvt_pk_f16_f32 v84, v84, v85
	v_cvt_pk_f16_f32 v85, v86, v87
	ds_write_b64 v246, v[84:85] offset:39168
	v_cvt_pk_f16_f32 v56, v56, v57
	v_cvt_pk_f16_f32 v57, v58, v59
	ds_write_b64 v246, v[56:57] offset:8704
	v_cvt_pk_f16_f32 v88, v88, v89
	v_cvt_pk_f16_f32 v89, v90, v91
	ds_write_b64 v246, v[88:89] offset:43520
	v_cvt_pk_f16_f32 v60, v60, v61
	v_cvt_pk_f16_f32 v61, v62, v63
	ds_write_b64 v246, v[60:61] offset:13056
	v_cvt_pk_f16_f32 v92, v92, v93
	v_cvt_pk_f16_f32 v93, v94, v95
	ds_write_b64 v246, v[92:93] offset:47872
	v_cvt_pk_f16_f32 v64, v64, v65
	v_cvt_pk_f16_f32 v65, v66, v67
	ds_write_b64 v246, v[64:65] offset:17408
	v_cvt_pk_f16_f32 v96, v96, v97
	v_cvt_pk_f16_f32 v97, v98, v99
	ds_write_b64 v246, v[96:97] offset:52224
	v_cvt_pk_f16_f32 v68, v68, v69
	v_cvt_pk_f16_f32 v69, v70, v71
	ds_write_b64 v246, v[68:69] offset:21760
	v_cvt_pk_f16_f32 v100, v100, v101
	v_cvt_pk_f16_f32 v101, v102, v103
	ds_write_b64 v246, v[100:101] offset:56576
	v_cvt_pk_f16_f32 v72, v72, v73
	v_cvt_pk_f16_f32 v73, v74, v75
	ds_write_b64 v246, v[72:73] offset:26112
	v_cvt_pk_f16_f32 v104, v104, v105
	v_cvt_pk_f16_f32 v105, v106, v107
	ds_write_b64 v246, v[104:105] offset:60928
	v_cvt_pk_f16_f32 v76, v76, v77
	v_cvt_pk_f16_f32 v77, v78, v79
	ds_write_b64 v246, v[76:77] offset:30464
	v_cvt_pk_f16_f32 v108, v108, v109
	v_cvt_pk_f16_f32 v109, v110, v111
	ds_write_b64 v246, v[108:109] offset:65280
	s_branch .LBB0_15
